# speedup vs baseline: 1.0041x; 1.0041x over previous
.Ls1_join:
	s_barrier
	s_setprio 1
	v_mfma_f32_16x16x32_f16 v[30:33], v[208:211], v[176:179], v[30:33]
	v_mfma_f32_16x16x32_f16 v[26:29], v[216:219], v[176:179], v[26:29]
	v_mfma_f32_16x16x32_f16 v[22:25], v[208:211], v[184:187], v[22:25]
	v_mfma_f32_16x16x32_f16 v[18:21], v[216:219], v[184:187], v[18:21]
	v_mfma_f32_16x16x32_f16 v[14:17], v[208:211], v[192:195], v[14:17]
	v_mfma_f32_16x16x32_f16 v[10:13], v[216:219], v[192:195], v[10:13]
	v_mfma_f32_16x16x32_f16 v[6:9], v[208:211], v[200:203], v[6:9]
	v_mfma_f32_16x16x32_f16 v[2:5], v[216:219], v[200:203], v[2:5]
	v_mfma_f32_16x16x32_f16 v[30:33], v[212:215], v[180:183], v[30:33]
	v_mfma_f32_16x16x32_f16 v[26:29], v[220:223], v[180:183], v[26:29]
	v_mfma_f32_16x16x32_f16 v[22:25], v[212:215], v[188:191], v[22:25]
	v_mfma_f32_16x16x32_f16 v[18:21], v[220:223], v[188:191], v[18:21]
	v_mfma_f32_16x16x32_f16 v[14:17], v[212:215], v[196:199], v[14:17]
	v_mfma_f32_16x16x32_f16 v[10:13], v[220:223], v[196:199], v[10:13]
	v_mfma_f32_16x16x32_f16 v[6:9], v[212:215], v[204:207], v[6:9]
	v_mfma_f32_16x16x32_f16 v[2:5], v[220:223], v[204:207], v[2:5]
	s_setprio 0
	s_barrier
	ds_read_b128 v[160:163], v143
	ds_read_b128 v[164:167], v143 offset:1024
	ds_read_b128 v[168:171], v143 offset:2048
	ds_read_b128 v[172:175], v143 offset:3072
	s_add_u32 s24, s18, s2
	s_addc_u32 s25, s19, s3
	v_readfirstlane_b32 s33, v148
	v_lshl_add_u64 v[208:209], s[24:25], 0, v[132:133]
	s_mov_b32 m0, s33
	ds_read_b128 v[176:179], v138 offset:32768
	ds_read_b128 v[180:183], v138 offset:33792
	ds_read_b128 v[184:187], v137 offset:32768
	ds_read_b128 v[188:191], v137 offset:33792
	ds_read_b128 v[192:195], v136 offset:32768
	ds_read_b128 v[196:199], v136 offset:33792
	ds_read_b128 v[200:203], v135 offset:32768
	ds_read_b128 v[204:207], v135 offset:33792
	global_load_lds_dwordx4 v[208:209], off
	v_lshl_add_u64 v[208:209], s[24:25], 0, v[130:131]
	v_readfirstlane_b32 s24, v149
	s_mov_b32 m0, s24
	s_nop 0
	global_load_lds_dwordx4 v[208:209], off
	s_waitcnt lgkmcnt(8)
	s_barrier
	s_waitcnt lgkmcnt(0)
	s_setprio 1
	s_waitcnt lgkmcnt(0)
	v_mfma_f32_16x16x32_f16 v[126:129], v[160:163], v[176:179], v[126:129]
	v_mfma_f32_16x16x32_f16 v[122:125], v[168:171], v[176:179], v[122:125]
	v_mfma_f32_16x16x32_f16 v[118:121], v[160:163], v[184:187], v[118:121]
	v_mfma_f32_16x16x32_f16 v[114:117], v[168:171], v[184:187], v[114:117]
	v_mfma_f32_16x16x32_f16 v[110:113], v[160:163], v[192:195], v[110:113]
	v_mfma_f32_16x16x32_f16 v[106:109], v[168:171], v[192:195], v[106:109]
	v_mfma_f32_16x16x32_f16 v[102:105], v[160:163], v[200:203], v[102:105]
	v_mfma_f32_16x16x32_f16 v[98:101], v[168:171], v[200:203], v[98:101]
	v_mfma_f32_16x16x32_f16 v[126:129], v[164:167], v[180:183], v[126:129]
	v_mfma_f32_16x16x32_f16 v[122:125], v[172:175], v[180:183], v[122:125]
	v_mfma_f32_16x16x32_f16 v[118:121], v[164:167], v[188:191], v[118:121]
	v_mfma_f32_16x16x32_f16 v[114:117], v[172:175], v[188:191], v[114:117]
	v_mfma_f32_16x16x32_f16 v[110:113], v[164:167], v[196:199], v[110:113]
	v_mfma_f32_16x16x32_f16 v[106:109], v[172:175], v[196:199], v[106:109]
	v_mfma_f32_16x16x32_f16 v[102:105], v[164:167], v[204:207], v[102:105]
	v_mfma_f32_16x16x32_f16 v[98:101], v[172:175], v[204:207], v[98:101]
	s_setprio 0
	s_barrier
	s_add_u32 s24, s26, 0x180
	s_addc_u32 s25, s27, 0
	v_readfirstlane_b32 s26, v150
	v_lshl_add_u64 v[224:225], s[24:25], 0, v[132:133]
	s_mov_b32 m0, s26
	ds_read_b128 v[208:211], v139
	ds_read_b128 v[212:215], v139 offset:1024
	ds_read_b128 v[216:219], v139 offset:2048
	ds_read_b128 v[220:223], v139 offset:3072
	global_load_lds_dwordx4 v[224:225], off
	v_lshl_add_u64 v[224:225], s[24:25], 0, v[130:131]
	v_readfirstlane_b32 s24, v151
	s_mov_b32 m0, s24
	s_nop 0
	global_load_lds_dwordx4 v[224:225], off
	s_barrier
	s_waitcnt lgkmcnt(0)
	s_setprio 1
	s_waitcnt lgkmcnt(0)
	v_mfma_f32_16x16x32_f16 v[94:97], v[208:211], v[176:179], v[94:97]
	v_mfma_f32_16x16x32_f16 v[90:93], v[216:219], v[176:179], v[90:93]
	v_mfma_f32_16x16x32_f16 v[86:89], v[208:211], v[184:187], v[86:89]
	v_mfma_f32_16x16x32_f16 v[82:85], v[216:219], v[184:187], v[82:85]
	v_mfma_f32_16x16x32_f16 v[78:81], v[208:211], v[192:195], v[78:81]
	v_mfma_f32_16x16x32_f16 v[74:77], v[216:219], v[192:195], v[74:77]
	v_mfma_f32_16x16x32_f16 v[70:73], v[208:211], v[200:203], v[70:73]
	v_mfma_f32_16x16x32_f16 v[66:69], v[216:219], v[200:203], v[66:69]
	v_mfma_f32_16x16x32_f16 v[94:97], v[212:215], v[180:183], v[94:97]
	v_mfma_f32_16x16x32_f16 v[90:93], v[220:223], v[180:183], v[90:93]
	v_mfma_f32_16x16x32_f16 v[86:89], v[212:215], v[188:191], v[86:89]
	v_mfma_f32_16x16x32_f16 v[82:85], v[220:223], v[188:191], v[82:85]
	v_mfma_f32_16x16x32_f16 v[78:81], v[212:215], v[196:199], v[78:81]
	v_mfma_f32_16x16x32_f16 v[74:77], v[220:223], v[196:199], v[74:77]
	v_mfma_f32_16x16x32_f16 v[70:73], v[212:215], v[204:207], v[70:73]
	v_mfma_f32_16x16x32_f16 v[66:69], v[220:223], v[204:207], v[66:69]
	s_setprio 0
	s_add_u32 s24, s28, 0x180
	s_addc_u32 s25, s29, 0
	v_readfirstlane_b32 s26, v152
	v_lshl_add_u64 v[224:225], s[24:25], 0, v[132:133]
	s_mov_b32 m0, s26
	s_barrier
	ds_read_b128 v[176:179], v138 offset:49152
	ds_read_b128 v[180:183], v138 offset:50176
	ds_read_b128 v[184:187], v137 offset:49152
	ds_read_b128 v[188:191], v137 offset:50176
	ds_read_b128 v[192:195], v136 offset:49152
	ds_read_b128 v[196:199], v136 offset:50176
	ds_read_b128 v[200:203], v135 offset:49152
	ds_read_b128 v[204:207], v135 offset:50176
	global_load_lds_dwordx4 v[224:225], off
	v_lshl_add_u64 v[224:225], s[24:25], 0, v[130:131]
	v_readfirstlane_b32 s24, v154
	s_mov_b32 m0, s24
	s_nop 0
	global_load_lds_dwordx4 v[224:225], off
	s_barrier
	s_waitcnt lgkmcnt(0)
	s_setprio 1
	s_waitcnt lgkmcnt(0)
	v_mfma_f32_16x16x32_f16 v[62:65], v[160:163], v[176:179], v[62:65]
	v_mfma_f32_16x16x32_f16 v[58:61], v[168:171], v[176:179], v[58:61]
	v_mfma_f32_16x16x32_f16 v[54:57], v[160:163], v[184:187], v[54:57]
	v_mfma_f32_16x16x32_f16 v[50:53], v[168:171], v[184:187], v[50:53]
	v_mfma_f32_16x16x32_f16 v[46:49], v[160:163], v[192:195], v[46:49]
	v_mfma_f32_16x16x32_f16 v[42:45], v[168:171], v[192:195], v[42:45]
	v_mfma_f32_16x16x32_f16 v[38:41], v[160:163], v[200:203], v[38:41]
	v_mfma_f32_16x16x32_f16 v[34:37], v[168:171], v[200:203], v[34:37]
	v_mfma_f32_16x16x32_f16 v[62:65], v[164:167], v[180:183], v[62:65]
	v_mfma_f32_16x16x32_f16 v[58:61], v[172:175], v[180:183], v[58:61]
	v_mfma_f32_16x16x32_f16 v[54:57], v[164:167], v[188:191], v[54:57]
	v_mfma_f32_16x16x32_f16 v[50:53], v[172:175], v[188:191], v[50:53]
	v_mfma_f32_16x16x32_f16 v[46:49], v[164:167], v[196:199], v[46:49]
	v_mfma_f32_16x16x32_f16 v[42:45], v[172:175], v[196:199], v[42:45]
	v_mfma_f32_16x16x32_f16 v[38:41], v[164:167], v[204:207], v[38:41]
	v_mfma_f32_16x16x32_f16 v[34:37], v[172:175], v[204:207], v[34:37]
	s_setprio 0
	s_barrier
	s_add_u32 s24, s30, 0x180
	s_addc_u32 s25, s31, 0
	v_readfirstlane_b32 s26, v155
	v_lshl_add_u64 v[160:161], s[24:25], 0, v[132:133]
	s_mov_b32 m0, s26
	s_nop 0
	global_load_lds_dwordx4 v[160:161], off
	v_lshl_add_u64 v[160:161], s[24:25], 0, v[130:131]
	v_readfirstlane_b32 s24, v156
	s_mov_b32 m0, s24
	s_nop 0
	global_load_lds_dwordx4 v[160:161], off
	s_cmp_eq_u32 s49, 9
	s_cbranch_scc1 .Ls2_arr2
	s_cmp_eq_u32 s49, 12
	s_cbranch_scc1 .Ls2_poll2
	s_cmp_eq_u32 s49, 18
	s_cbranch_scc1 .Ls2_arr3
	s_cmp_eq_u32 s49, 21
	s_cbranch_scc1 .Ls2_poll3
	s_cmp_eq_u32 s49, 11
	s_cbranch_scc1 .Ls2_pf2
	s_cmp_eq_u32 s49, 20
	s_cbranch_scc1 .Ls2_pf3

.Ls2_pf2:
	s_and_saveexec_b64 s[52:53], s[56:57]
	s_cbranch_execz .Ls2_pf2_no
	v_mov_b32_e32 v238, 0
	global_load_dword v239, v238, s[54:55] offset:64 sc1
	s_or_b64 exec, exec, s[52:53]
	s_waitcnt vmcnt(7)
	s_branch .Ls2_join

.Ls2_pf3:
	s_and_saveexec_b64 s[52:53], s[56:57]
	s_cbranch_execz .Ls2_pf3_no
	v_mov_b32_e32 v238, 0
	global_load_dword v239, v238, s[54:55] offset:128 sc1
	s_or_b64 exec, exec, s[52:53]
	s_waitcnt vmcnt(7)
	s_branch .Ls2_join

.Ls2_poll2:
	s_cmp_eq_u64 s[56:57], 0
	s_cbranch_scc1 .Ls2_plain
	s_mov_b32 s58, 0
	v_mov_b32_e32 v238, 0
	s_waitcnt vmcnt(16)
	v_readfirstlane_b32 s59, v239
	s_cmp_ge_u32 s59, 0x100
	s_cbranch_scc1 .Ls2_plain
